# router epilogue: the 20 router bias values are loaded once per phase into VGPR lanes and read with v_readlane instead of up to 17 serialized global loads per 4-row group
# baseline (speedup 1.0000x reference)
.LBB0_2246:
	s_or_b64 exec, exec, s[2:3]
	s_and_saveexec_b64 s[30:31], vcc
	s_cbranch_execz .LBB0_2293
	v_and_b32_e32 v7, 8, v15
	v_cmp_eq_u32_e64 s[10:11], 0, v7
	v_and_b32_e32 v7, 4, v15
	s_movk_i32 s0, 0x150
	v_cmp_eq_u32_e64 s[12:13], 0, v7
	v_and_b32_e32 v7, 3, v15
	v_mul_lo_u32 v5, v73, s0
	v_readlane_b32 s0, v253, 39
	v_cmp_eq_u32_e64 s[14:15], 0, v7
	v_lshrrev_b32_e32 v7, 3, v15
	v_lshrrev_b32_e32 v11, 1, v15
	v_add_u32_e32 v5, s0, v5
	v_and_b32_e32 v7, 4, v7
	v_and_b32_e32 v11, 8, v11
	v_add3_u32 v7, v5, v7, v11
	v_lshlrev_b32_e32 v11, 1, v15
	v_and_b32_e32 v11, 16, v11
	v_and_b32_e32 v2, 32, v2
	v_readlane_b32 s0, v252, 54
	v_and_b32_e32 v6, 32, v15
	v_add3_u32 v19, v7, v11, v2
	v_readlane_b32 s1, v252, 55
	v_lshlrev_b32_e32 v2, 5, v75
	v_lshlrev_b32_e32 v13, 2, v73
	v_cmp_eq_u32_e64 s[6:7], 0, v6
	v_and_b32_e32 v6, 16, v15
	v_readlane_b32 s1, v253, 55
	v_add3_u32 v73, v2, v13, s69
	v_lshrrev_b32_e32 v2, 1, v75
	v_lshl_add_u32 v9, v75, 4, 0
	v_cmp_eq_u32_e64 s[8:9], 0, v6
	v_lshlrev_b32_e32 v6, 2, v75
	v_lshrrev_b32_e32 v7, 2, v75
	v_mul_lo_u32 v23, v75, s0
	v_mul_u32_u24_e32 v11, 0x50, v75
	s_lshl_b32 s0, s1, 2
	s_lshl_b32 s50, s1, 4
	s_mov_b32 s1, s51
	v_and_or_b32 v2, v2, 24, 32
	v_readlane_b32 s2, v252, 5
	s_mov_b32 s44, 0
	v_cmp_eq_u32_e64 s[16:17], 0, v4
	v_cmp_gt_u32_e64 s[18:19], 4, v75
	v_add_u32_e32 v25, v5, v6
	v_add_u32_e32 v27, 0x10000, v9
	v_add_u32_e32 v33, 0x10400, v9
	v_add_u32_e32 v35, 0x10800, v9
	v_add_u32_e32 v37, 0x10c00, v9
	v_add_u32_e32 v41, 0x11000, v9
	v_add_u32_e32 v43, 0x11400, v9
	v_add_u32_e32 v45, 0x11800, v9
	v_add_u32_e32 v49, 0x11c00, v9
	v_add_u32_e32 v51, 0x12000, v9
	v_add_u32_e32 v53, 0x12400, v9
	v_add_u32_e32 v57, 0x12800, v9
	v_add_u32_e32 v59, 0x12c00, v9
	v_add_u32_e32 v61, 0x13000, v9
	v_add_u32_e32 v65, 0x13400, v9
	v_add_u32_e32 v67, 0x13800, v9
	v_add_u32_e32 v69, 0x13c00, v9
	v_mul_lo_u32 v75, s2, v2
	s_mov_b64 s[34:35], 0
	v_lshlrev_b32_e32 v2, 1, v6
	v_lshlrev_b32_e32 v30, 2, v4
	v_add_u32_e32 v77, v5, v7
	s_lshl_b64 s[36:37], s[0:1], 2
	v_add_u32_e32 v81, v5, v11
	s_load_dwordx2 s[100:101], s[26:27], 0xb8
	v_and_b32_e32 v240, 15, v0
	v_add_u32_e32 v240, s50, v240
	v_lshlrev_b32_e32 v240, 2, v240
	v_and_b32_e32 v241, 3, v0
	v_lshlrev_b32_e32 v241, 2, v241
	v_add_u32_e32 v241, s36, v241
	s_waitcnt lgkmcnt(0)
	global_load_dword v240, v240, s[100:101]
	s_load_dwordx2 s[100:101], s[26:27], 0xa8
	s_waitcnt lgkmcnt(0)
	global_load_dword v241, v241, s[100:101]
	s_waitcnt vmcnt(0)
	v_mov_b32_e32 v11, v83
	s_branch .LBB0_2249

.LBB0_2255:
	s_or_b64 exec, exec, s[2:3]
	s_waitcnt lgkmcnt(0)
	s_and_saveexec_b64 s[38:39], s[18:19]
	s_cbranch_execz .LBB0_2248
	s_load_dwordx2 s[2:3], s[26:27], 0xa8
	s_load_dwordx2 s[40:41], s[26:27], 0xb8
	s_waitcnt lgkmcnt(0)
	s_add_u32 s2, s2, s36
	s_addc_u32 s3, s3, s37
	v_readlane_b32 s100, v241, 0
	v_readlane_b32 s101, v241, 1
	v_mov_b32_e32 v4, s100
	v_mov_b32_e32 v5, s101
	v_readlane_b32 s100, v241, 2
	v_readlane_b32 s101, v241, 3
	v_mov_b32_e32 v6, s100
	v_mov_b32_e32 v7, s101
	ds_read_b32 v142, v25 offset:320
	ds_read_b128 v[158:161], v81
	ds_read2_b32 v[156:157], v81 offset0:5 offset1:6
	ds_read2_b32 v[148:149], v81 offset0:7 offset1:8
	ds_read2_b32 v[154:155], v81 offset0:9 offset1:10
	ds_read2_b32 v[146:147], v81 offset0:11 offset1:12
	ds_read2_b32 v[152:153], v81 offset0:13 offset1:14
	ds_read2_b32 v[144:145], v81 offset0:15 offset1:16
	ds_read2_b32 v[150:151], v81 offset0:17 offset1:18
	ds_read_b32 v31, v81 offset:76
	s_waitcnt lgkmcnt(8)
	v_pk_fma_f32 v[4:5], v[142:143], v[158:159], v[4:5] op_sel_hi:[0,1,1]
	v_cmp_gt_f32_e32 vcc, v5, v4
	v_fma_f32 v13, v142, v160, v6
	v_fmac_f32_e32 v7, v142, v161
	v_cndmask_b32_e32 v6, v4, v5, vcc
	v_cmp_gt_f32_e64 s[22:23], v13, v6
	v_cndmask_b32_e64 v21, 0, 1, vcc
	s_nop 0
	v_cndmask_b32_e64 v29, v6, v13, s[22:23]
	v_cndmask_b32_e64 v6, v21, 2, s[22:23]
	v_cmp_ngt_f32_e32 vcc, v7, v29
	v_cmp_gt_f32_e64 s[2:3], v7, v29
	v_mov_b32_e32 v21, 0
	v_cndmask_b32_e32 v6, 3, v6, vcc
	v_cmp_eq_u32_e64 s[4:5], 0, v6
	s_and_saveexec_b64 s[20:21], s[4:5]
	s_cbranch_execz .LBB0_2272
	s_lshl_b64 s[42:43], s[50:51], 2
	s_add_u32 s42, s40, s42
	s_addc_u32 s43, s41, s43
	v_readlane_b32 s100, v240, 0
	s_nop 0
	v_mov_b32_e32 v21, s100
	ds_read_b32 v39, v81 offset:16
	s_waitcnt lgkmcnt(0)
	v_fmac_f32_e32 v21, v142, v39
	s_or_b64 exec, exec, s[20:21]
	v_cmp_eq_u32_e64 s[20:21], 1, v6
	s_and_saveexec_b64 s[42:43], s[20:21]
	s_cbranch_execnz .LBB0_2273

.LBB0_2259:
	s_lshl_b64 s[46:47], s[50:51], 2
	s_add_u32 s46, s40, s46
	s_addc_u32 s47, s41, s47
	v_readlane_b32 s100, v240, 8
	s_nop 0
	v_mov_b32_e32 v21, s100
	s_waitcnt lgkmcnt(4)
	v_fmac_f32_e32 v21, v142, v147
	s_or_b64 exec, exec, s[42:43]
	s_and_saveexec_b64 s[42:43], s[2:3]
	s_cbranch_execnz .LBB0_2275

.LBB0_2261:
	s_lshl_b64 s[46:47], s[50:51], 2
	s_add_u32 s46, s40, s46
	s_addc_u32 s47, s41, s47
	v_readlane_b32 s100, v240, 1
	s_nop 0
	v_mov_b32_e32 v39, s100
	s_waitcnt lgkmcnt(7)
	v_fmac_f32_e32 v39, v142, v156
	s_or_b64 exec, exec, s[42:43]
	s_and_saveexec_b64 s[42:43], s[20:21]
	s_cbranch_execnz .LBB0_2277

.LBB0_2263:
	s_lshl_b64 s[46:47], s[50:51], 2
	s_add_u32 s46, s40, s46
	s_addc_u32 s47, s41, s47
	v_readlane_b32 s100, v240, 9
	s_nop 0
	v_mov_b32_e32 v39, s100
	s_waitcnt lgkmcnt(3)
	v_fmac_f32_e32 v39, v142, v152
	s_or_b64 exec, exec, s[42:43]
	s_and_saveexec_b64 s[42:43], s[2:3]
	s_cbranch_execnz .LBB0_2279

.LBB0_2265:
	s_lshl_b64 s[46:47], s[50:51], 2
	s_add_u32 s46, s40, s46
	s_addc_u32 s47, s41, s47
	v_readlane_b32 s100, v240, 2
	s_nop 0
	v_mov_b32_e32 v47, s100
	s_waitcnt lgkmcnt(7)
	v_fmac_f32_e32 v47, v142, v157
	s_or_b64 exec, exec, s[42:43]
	s_and_saveexec_b64 s[42:43], s[20:21]
	s_cbranch_execnz .LBB0_2281

.LBB0_2267:
	s_lshl_b64 s[46:47], s[50:51], 2
	s_add_u32 s46, s40, s46
	s_addc_u32 s47, s41, s47
	v_readlane_b32 s100, v240, 10
	s_nop 0
	v_mov_b32_e32 v47, s100
	s_waitcnt lgkmcnt(3)
	v_fmac_f32_e32 v47, v142, v153
	s_or_b64 exec, exec, s[42:43]
	s_and_saveexec_b64 s[42:43], s[2:3]
	s_cbranch_execnz .LBB0_2283

.LBB0_2269:
	s_lshl_b64 s[4:5], s[50:51], 2
	s_add_u32 s4, s40, s4
	s_addc_u32 s5, s41, s5
	v_readlane_b32 s100, v240, 3
	s_nop 0
	v_mov_b32_e32 v55, s100
	s_waitcnt lgkmcnt(6)
	v_fmac_f32_e32 v55, v142, v148
	s_or_b64 exec, exec, s[42:43]
	s_and_saveexec_b64 s[4:5], s[20:21]
	s_cbranch_execnz .LBB0_2285

.LBB0_2271:
	s_lshl_b64 s[20:21], s[50:51], 2
	s_add_u32 s20, s40, s20
	s_addc_u32 s21, s41, s21
	v_readlane_b32 s100, v240, 11
	s_nop 0
	v_mov_b32_e32 v55, s100
	s_waitcnt lgkmcnt(2)
	v_fmac_f32_e32 v55, v142, v144
	s_or_b64 exec, exec, s[4:5]
	s_and_saveexec_b64 s[4:5], s[2:3]
	s_cbranch_execnz .LBB0_2287
	s_branch .LBB0_2288

.LBB0_2273:
	s_lshl_b64 s[46:47], s[50:51], 2
	s_add_u32 s46, s40, s46
	s_addc_u32 s47, s41, s47
	v_readlane_b32 s100, v240, 4
	s_nop 0
	v_mov_b32_e32 v21, s100
	s_waitcnt lgkmcnt(6)
	v_fmac_f32_e32 v21, v142, v149
	s_or_b64 exec, exec, s[42:43]
	s_and_b64 s[22:23], s[22:23], vcc
	s_and_saveexec_b64 s[42:43], s[22:23]
	s_cbranch_execnz .LBB0_2259

.LBB0_2275:
	s_lshl_b64 s[46:47], s[50:51], 2
	s_add_u32 s46, s40, s46
	s_addc_u32 s47, s41, s47
	v_readlane_b32 s100, v240, 12
	s_nop 0
	v_mov_b32_e32 v21, s100
	s_waitcnt lgkmcnt(2)
	v_fmac_f32_e32 v21, v142, v145
	s_or_b64 exec, exec, s[42:43]
	v_mov_b32_e32 v39, 0
	s_and_saveexec_b64 s[42:43], s[4:5]
	s_cbranch_execnz .LBB0_2261

.LBB0_2277:
	s_lshl_b64 s[46:47], s[50:51], 2
	s_add_u32 s46, s40, s46
	s_addc_u32 s47, s41, s47
	v_readlane_b32 s100, v240, 5
	s_nop 0
	v_mov_b32_e32 v39, s100
	s_waitcnt lgkmcnt(5)
	v_fmac_f32_e32 v39, v142, v154
	s_or_b64 exec, exec, s[42:43]
	s_and_saveexec_b64 s[42:43], s[22:23]
	s_cbranch_execnz .LBB0_2263

.LBB0_2279:
	s_lshl_b64 s[46:47], s[50:51], 2
	s_add_u32 s46, s40, s46
	s_addc_u32 s47, s41, s47
	v_readlane_b32 s100, v240, 13
	s_nop 0
	v_mov_b32_e32 v39, s100
	s_waitcnt lgkmcnt(1)
	v_fmac_f32_e32 v39, v142, v150
	s_or_b64 exec, exec, s[42:43]
	v_mov_b32_e32 v47, 0
	s_and_saveexec_b64 s[42:43], s[4:5]
	s_cbranch_execnz .LBB0_2265

.LBB0_2281:
	s_lshl_b64 s[46:47], s[50:51], 2
	s_add_u32 s46, s40, s46
	s_addc_u32 s47, s41, s47
	v_readlane_b32 s100, v240, 6
	s_nop 0
	v_mov_b32_e32 v47, s100
	s_waitcnt lgkmcnt(5)
	v_fmac_f32_e32 v47, v142, v155
	s_or_b64 exec, exec, s[42:43]
	s_and_saveexec_b64 s[42:43], s[22:23]
	s_cbranch_execnz .LBB0_2267

.LBB0_2283:
	s_lshl_b64 s[46:47], s[50:51], 2
	s_add_u32 s46, s40, s46
	s_addc_u32 s47, s41, s47
	v_readlane_b32 s100, v240, 14
	s_nop 0
	v_mov_b32_e32 v47, s100
	s_waitcnt lgkmcnt(1)
	v_fmac_f32_e32 v47, v142, v151
	s_or_b64 exec, exec, s[42:43]
	v_mov_b32_e32 v55, 0
	s_and_saveexec_b64 s[42:43], s[4:5]
	s_cbranch_execnz .LBB0_2269

.LBB0_2285:
	s_lshl_b64 s[20:21], s[50:51], 2
	s_add_u32 s20, s40, s20
	s_addc_u32 s21, s41, s21
	v_readlane_b32 s100, v240, 7
	s_nop 0
	v_mov_b32_e32 v55, s100
	s_waitcnt lgkmcnt(4)
	v_fmac_f32_e32 v55, v142, v146
	s_or_b64 exec, exec, s[4:5]
	s_and_saveexec_b64 s[4:5], s[22:23]
	s_cbranch_execnz .LBB0_2271

.LBB0_2287:
	s_lshl_b64 s[2:3], s[50:51], 2
	s_add_u32 s2, s40, s2
	s_addc_u32 s3, s41, s3
	v_readlane_b32 s100, v240, 15
	s_nop 0
	v_mov_b32_e32 v55, s100
	s_waitcnt lgkmcnt(0)
	v_fmac_f32_e32 v55, v142, v31
